# grid barrier: L1 invalidate issued before the spin (8 seams)
# speedup vs baseline: 1.0366x; 1.0076x over previous
; __device__ __forceinline__ unsigned xb_ld(unsigned* p)              { return __hip_atomic_load(p, __ATOMIC_RELAXED, __HIP_MEMORY_SCOPE_AGENT); }
; __device__ __forceinline__ unsigned xb_add(unsigned* p, unsigned v) { return __hip_atomic_fetch_add(p, v, __ATOMIC_RELAXED, __HIP_MEMORY_SCOPE_AGENT); }
; #define XB_SPIN(cond, bar) do { unsigned _sp = 0; while (cond) { __builtin_amdgcn_s_sleep(1); \
;     if ((++_sp & 255u) == 0u) { if (xb_ld(&(bar)[XB_TMO])) break; if (_sp > XB_SPIN_CAP) { atomicAdd(&(bar)[XB_TMO], 1u); break; } } } } while (0)
; __device__ __forceinline__ void xcd_barrier(const XcdBarrier& b, int tid) {
;     ...
;         const unsigned old = xb_add(&bar[XB_XSUB(b.x)], 1u);
;         const unsigned gen = old / nloc;
;         if (old + 1u == (gen + 1u) * nloc) {
;             __builtin_amdgcn_fence(__ATOMIC_RELEASE, "agent");
;             asm volatile("s_waitcnt vmcnt(0)" ::: "memory");
;             const unsigned og = xb_add(&bar[XB_TOP], 1u);
;             const unsigned tg = og / nx;
;             if (og + 1u == (tg + 1u) * nx) xb_add(&bar[XB_TOPGEN], 1u);
;             else XB_SPIN(xb_ld(&bar[XB_TOPGEN]) == tg, bar);
;             __builtin_amdgcn_fence(__ATOMIC_ACQUIRE, "agent");
;             xb_add(&bar[XB_XGEN(b.x)], 1u);
;             asm volatile("s_waitcnt vmcnt(0)" ::: "memory");
;         } else {
;             XB_SPIN(xb_ld(&bar[XB_XGEN(b.x)]) == gen, bar);
;             __builtin_amdgcn_fence(__ATOMIC_ACQUIRE, "agent");
;             asm volatile("s_waitcnt vmcnt(0)" ::: "memory");
;         }
.LBB0_105:
	v_readlane_b32 s0, v249, 2
	s_lshl_b32 s0, s0, 8
	v_readlane_b32 s2, v249, 3
	v_readlane_b32 s3, v249, 4
	s_add_u32 s8, s2, s0
	s_addc_u32 s9, s3, 0
	v_mov_b32_e32 v1, 0x1000
	v_mov_b32_e32 v3, 1
	global_atomic_add v3, v1, v3, s[8:9] offset:1024 sc0
	v_cvt_f32_u32_e32 v1, v2
	v_sub_u32_e32 v4, 0, v2
	v_rcp_iflag_f32_e32 v1, v1
	s_nop 0
	v_mul_f32_e32 v1, 0x4f7ffffe, v1
	v_cvt_u32_f32_e32 v1, v1
	v_mul_lo_u32 v4, v4, v1
	v_mul_hi_u32 v4, v1, v4
	v_add_u32_e32 v1, v1, v4
	s_waitcnt vmcnt(0)
	v_mul_hi_u32 v1, v3, v1
	v_mul_lo_u32 v4, v1, v2
	v_sub_u32_e32 v4, v3, v4
	v_add_u32_e32 v5, 1, v1
	v_cmp_ge_u32_e32 vcc, v4, v2
	v_add_u32_e32 v3, 1, v3
	s_nop 0
	v_cndmask_b32_e32 v1, v1, v5, vcc
	v_sub_u32_e32 v5, v4, v2
	v_cndmask_b32_e32 v4, v4, v5, vcc
	v_add_u32_e32 v5, 1, v1
	v_cmp_ge_u32_e32 vcc, v4, v2
	s_nop 1
	v_cndmask_b32_e32 v1, v1, v5, vcc
	v_mul_lo_u32 v4, v2, v1
	v_add_u32_e32 v2, v4, v2
	v_cmp_ne_u32_e32 vcc, v3, v2
	s_and_saveexec_b64 s[0:1], vcc
	s_xor_b64 s[10:11], exec, s[0:1]
	s_cbranch_execz .LBB0_119
	s_waitcnt lgkmcnt(0)
	buffer_inv sc1
	v_mov_b32_e32 v0, 0x2000
	global_load_dword v0, v0, s[8:9] offset:1024 sc1
	s_add_u32 s16, s8, 0x2400
	s_addc_u32 s17, s9, 0
	s_waitcnt vmcnt(0)
	v_cmp_eq_u32_e32 vcc, v0, v1
	s_and_saveexec_b64 s[12:13], vcc
	s_cbranch_execz .LBB0_118
	s_add_u32 s14, s84, 0x4200
	s_addc_u32 s15, s85, 0
	s_mov_b32 s2, 1
	s_mov_b64 s[18:19], 0
	v_mov_b32_e32 v0, 0
	s_branch .LBB0_109

; __device__ __forceinline__ unsigned xb_ld(unsigned* p)              { return __hip_atomic_load(p, __ATOMIC_RELAXED, __HIP_MEMORY_SCOPE_AGENT); }
; #define XB_SPIN(cond, bar) do { unsigned _sp = 0; while (cond) { __builtin_amdgcn_s_sleep(1); \
;     if ((++_sp & 255u) == 0u) { if (xb_ld(&(bar)[XB_TMO])) break; if (_sp > XB_SPIN_CAP) { atomicAdd(&(bar)[XB_TMO], 1u); break; } } } } while (0)
; __device__ __forceinline__ void xcd_barrier(const XcdBarrier& b, int tid) {
;     ...
;             XB_SPIN(xb_ld(&bar[XB_XGEN(b.x)]) == gen, bar);
;             __builtin_amdgcn_fence(__ATOMIC_ACQUIRE, "agent");
;             asm volatile("s_waitcnt vmcnt(0)" ::: "memory");
.LBB0_118:
	s_or_b64 exec, exec, s[12:13]
	s_waitcnt vmcnt(0)
	s_waitcnt vmcnt(0)

; __device__ __forceinline__ unsigned xb_ld(unsigned* p)              { return __hip_atomic_load(p, __ATOMIC_RELAXED, __HIP_MEMORY_SCOPE_AGENT); }
; __device__ __forceinline__ unsigned xb_add(unsigned* p, unsigned v) { return __hip_atomic_fetch_add(p, v, __ATOMIC_RELAXED, __HIP_MEMORY_SCOPE_AGENT); }
; #define XB_SPIN(cond, bar) do { unsigned _sp = 0; while (cond) { __builtin_amdgcn_s_sleep(1); \
;     if ((++_sp & 255u) == 0u) { if (xb_ld(&(bar)[XB_TMO])) break; if (_sp > XB_SPIN_CAP) { atomicAdd(&(bar)[XB_TMO], 1u); break; } } } } while (0)
; __device__ __forceinline__ void xcd_barrier(const XcdBarrier& b, int tid) {
;     ...
;         if (old + 1u == (gen + 1u) * nloc) {
;             __builtin_amdgcn_fence(__ATOMIC_RELEASE, "agent");
;             asm volatile("s_waitcnt vmcnt(0)" ::: "memory");
;             const unsigned og = xb_add(&bar[XB_TOP], 1u);
;             const unsigned tg = og / nx;
;             if (og + 1u == (tg + 1u) * nx) xb_add(&bar[XB_TOPGEN], 1u);
;             else XB_SPIN(xb_ld(&bar[XB_TOPGEN]) == tg, bar);
.LBB0_122:
	s_or_b64 exec, exec, s[10:11]
	v_cvt_f32_u32_e32 v3, v0
	s_waitcnt vmcnt(0)
	buffer_inv sc1
	v_readfirstlane_b32 s0, v2
	s_add_u32 s12, s84, 0x7500
	s_addc_u32 s13, s85, 0
	v_rcp_iflag_f32_e32 v3, v3
	v_add_u32_e32 v1, s0, v1
	v_add_u32_e32 v4, 1, v1
	s_mov_b64 s[0:1], -1
	v_mul_f32_e32 v2, 0x4f7ffffe, v3
	v_cvt_u32_f32_e32 v2, v2
	v_sub_u32_e32 v3, 0, v0
	v_mul_lo_u32 v3, v3, v2
	v_mul_hi_u32 v3, v2, v3
	v_add_u32_e32 v2, v2, v3
	v_mul_hi_u32 v2, v1, v2
	v_mul_lo_u32 v3, v2, v0
	v_sub_u32_e32 v1, v1, v3
	v_add_u32_e32 v5, 1, v2
	v_cmp_ge_u32_e32 vcc, v1, v0
	v_sub_u32_e32 v3, v1, v0
	s_nop 0
	v_cndmask_b32_e32 v2, v2, v5, vcc
	v_cndmask_b32_e32 v1, v1, v3, vcc
	v_add_u32_e32 v3, 1, v2
	v_cmp_ge_u32_e32 vcc, v1, v0
	s_nop 1
	v_cndmask_b32_e32 v2, v2, v3, vcc
	v_mul_lo_u32 v1, v0, v2
	v_add_u32_e32 v0, v1, v0
	v_cmp_ne_u32_e32 vcc, v4, v0
	v_mov_b64_e32 v[0:1], s[12:13]
	s_and_saveexec_b64 s[10:11], vcc
	s_cbranch_execz .LBB0_134
	v_mov_b32_e32 v0, 0
	global_load_dword v1, v0, s[12:13] sc1
	s_mov_b64 s[0:1], 0
	s_waitcnt vmcnt(0)
	v_cmp_eq_u32_e32 vcc, v1, v2
	s_and_saveexec_b64 s[16:17], vcc
	s_cbranch_execz .LBB0_133
	s_add_u32 s14, s84, 0x4200
	s_addc_u32 s15, s85, 0
	s_mov_b32 s2, 1
	s_mov_b64 s[18:19], 0
	s_branch .LBB0_126

; __device__ __forceinline__ unsigned xb_ld(unsigned* p)              { return __hip_atomic_load(p, __ATOMIC_RELAXED, __HIP_MEMORY_SCOPE_AGENT); }
; __device__ __forceinline__ unsigned xb_add(unsigned* p, unsigned v) { return __hip_atomic_fetch_add(p, v, __ATOMIC_RELAXED, __HIP_MEMORY_SCOPE_AGENT); }
; #define XB_SPIN(cond, bar) do { unsigned _sp = 0; while (cond) { __builtin_amdgcn_s_sleep(1); \
;     if ((++_sp & 255u) == 0u) { if (xb_ld(&(bar)[XB_TMO])) break; if (_sp > XB_SPIN_CAP) { atomicAdd(&(bar)[XB_TMO], 1u); break; } } } } while (0)
; __device__ __forceinline__ void xcd_barrier(const XcdBarrier& b, int tid) {
;     ...
;             else XB_SPIN(xb_ld(&bar[XB_TOPGEN]) == tg, bar);
;             __builtin_amdgcn_fence(__ATOMIC_ACQUIRE, "agent");
;             xb_add(&bar[XB_XGEN(b.x)], 1u);
;             asm volatile("s_waitcnt vmcnt(0)" ::: "memory");
.LBB0_136:
	s_or_b64 exec, exec, s[10:11]
	v_mov_b32_e32 v0, 0x2000
	v_mov_b32_e32 v1, 1
	s_waitcnt vmcnt(0)
	global_atomic_add v0, v1, s[8:9] offset:1024
	s_waitcnt vmcnt(0)

; __device__ __forceinline__ unsigned xb_ld(unsigned* p)              { return __hip_atomic_load(p, __ATOMIC_RELAXED, __HIP_MEMORY_SCOPE_AGENT); }
; __device__ __forceinline__ unsigned xb_add(unsigned* p, unsigned v) { return __hip_atomic_fetch_add(p, v, __ATOMIC_RELAXED, __HIP_MEMORY_SCOPE_AGENT); }
; #define XB_SPIN(cond, bar) do { unsigned _sp = 0; while (cond) { __builtin_amdgcn_s_sleep(1); \
;     if ((++_sp & 255u) == 0u) { if (xb_ld(&(bar)[XB_TMO])) break; if (_sp > XB_SPIN_CAP) { atomicAdd(&(bar)[XB_TMO], 1u); break; } } } } while (0)
; __device__ __forceinline__ void xcd_barrier(const XcdBarrier& b, int tid) {
;     ...
;         const unsigned old = xb_add(&bar[XB_XSUB(b.x)], 1u);
;         const unsigned gen = old / nloc;
;         if (old + 1u == (gen + 1u) * nloc) {
;             __builtin_amdgcn_fence(__ATOMIC_RELEASE, "agent");
;             asm volatile("s_waitcnt vmcnt(0)" ::: "memory");
;             const unsigned og = xb_add(&bar[XB_TOP], 1u);
;             const unsigned tg = og / nx;
;             if (og + 1u == (tg + 1u) * nx) xb_add(&bar[XB_TOPGEN], 1u);
;             else XB_SPIN(xb_ld(&bar[XB_TOPGEN]) == tg, bar);
;             __builtin_amdgcn_fence(__ATOMIC_ACQUIRE, "agent");
;             xb_add(&bar[XB_XGEN(b.x)], 1u);
;             asm volatile("s_waitcnt vmcnt(0)" ::: "memory");
;         } else {
;             XB_SPIN(xb_ld(&bar[XB_XGEN(b.x)]) == gen, bar);
;             __builtin_amdgcn_fence(__ATOMIC_ACQUIRE, "agent");
;             asm volatile("s_waitcnt vmcnt(0)" ::: "memory");
;         }
.LBB0_1130:
	v_readlane_b32 s2, v249, 2
	s_lshl_b32 s2, s2, 8
	v_readlane_b32 s6, v249, 3
	v_readlane_b32 s7, v249, 4
	s_add_u32 s6, s6, s2
	s_addc_u32 s7, s7, 0
	v_mov_b32_e32 v1, 0x1000
	v_mov_b32_e32 v3, 1
	v_sub_u32_e32 v4, 0, v2
	global_atomic_add v3, v1, v3, s[6:7] offset:1024 sc0
	v_cvt_f32_u32_e32 v1, v2
	v_rcp_iflag_f32_e32 v1, v1
	s_nop 0
	v_mul_f32_e32 v1, 0x4f7ffffe, v1
	v_cvt_u32_f32_e32 v1, v1
	v_mul_lo_u32 v4, v4, v1
	v_mul_hi_u32 v4, v1, v4
	v_add_u32_e32 v1, v1, v4
	s_waitcnt vmcnt(0)
	v_mul_hi_u32 v1, v3, v1
	v_mul_lo_u32 v4, v1, v2
	v_sub_u32_e32 v4, v3, v4
	v_add_u32_e32 v5, 1, v1
	v_cmp_ge_u32_e32 vcc, v4, v2
	v_add_u32_e32 v3, 1, v3
	s_nop 0
	v_cndmask_b32_e32 v1, v1, v5, vcc
	v_sub_u32_e32 v5, v4, v2
	v_cndmask_b32_e32 v4, v4, v5, vcc
	v_add_u32_e32 v5, 1, v1
	v_cmp_ge_u32_e32 vcc, v4, v2
	s_nop 1
	v_cndmask_b32_e32 v1, v1, v5, vcc
	v_mul_lo_u32 v4, v2, v1
	v_add_u32_e32 v2, v4, v2
	v_cmp_ne_u32_e32 vcc, v3, v2
	s_and_saveexec_b64 s[2:3], vcc
	s_xor_b64 s[16:17], exec, s[2:3]
	s_cbranch_execz .LBB0_1144
	s_waitcnt lgkmcnt(0)
	buffer_inv sc1
	v_mov_b32_e32 v0, 0x2000
	global_load_dword v0, v0, s[6:7] offset:1024 sc1
	s_add_u32 s22, s6, 0x2400
	s_addc_u32 s23, s7, 0
	s_waitcnt vmcnt(0)
	v_cmp_eq_u32_e32 vcc, v0, v1
	s_and_saveexec_b64 s[18:19], vcc
	s_cbranch_execz .LBB0_1143
	s_add_u32 s20, s84, 0x4200
	s_addc_u32 s21, s85, 0
	s_mov_b32 s2, 1
	s_mov_b64 s[24:25], 0
	v_mov_b32_e32 v0, 0
	s_branch .LBB0_1134

; __device__ __forceinline__ unsigned xb_ld(unsigned* p)              { return __hip_atomic_load(p, __ATOMIC_RELAXED, __HIP_MEMORY_SCOPE_AGENT); }
; #define XB_SPIN(cond, bar) do { unsigned _sp = 0; while (cond) { __builtin_amdgcn_s_sleep(1); \
;     if ((++_sp & 255u) == 0u) { if (xb_ld(&(bar)[XB_TMO])) break; if (_sp > XB_SPIN_CAP) { atomicAdd(&(bar)[XB_TMO], 1u); break; } } } } while (0)
; __device__ __forceinline__ void xcd_barrier(const XcdBarrier& b, int tid) {
;     ...
;             XB_SPIN(xb_ld(&bar[XB_XGEN(b.x)]) == gen, bar);
;             __builtin_amdgcn_fence(__ATOMIC_ACQUIRE, "agent");
;             asm volatile("s_waitcnt vmcnt(0)" ::: "memory");
.LBB0_1143:
	s_or_b64 exec, exec, s[18:19]
	s_waitcnt vmcnt(0)
	s_waitcnt vmcnt(0)

; __device__ __forceinline__ unsigned xb_ld(unsigned* p)              { return __hip_atomic_load(p, __ATOMIC_RELAXED, __HIP_MEMORY_SCOPE_AGENT); }
; __device__ __forceinline__ unsigned xb_add(unsigned* p, unsigned v) { return __hip_atomic_fetch_add(p, v, __ATOMIC_RELAXED, __HIP_MEMORY_SCOPE_AGENT); }
; #define XB_SPIN(cond, bar) do { unsigned _sp = 0; while (cond) { __builtin_amdgcn_s_sleep(1); \
;     if ((++_sp & 255u) == 0u) { if (xb_ld(&(bar)[XB_TMO])) break; if (_sp > XB_SPIN_CAP) { atomicAdd(&(bar)[XB_TMO], 1u); break; } } } } while (0)
; __device__ __forceinline__ void xcd_barrier(const XcdBarrier& b, int tid) {
;     ...
;         if (old + 1u == (gen + 1u) * nloc) {
;             __builtin_amdgcn_fence(__ATOMIC_RELEASE, "agent");
;             asm volatile("s_waitcnt vmcnt(0)" ::: "memory");
;             const unsigned og = xb_add(&bar[XB_TOP], 1u);
;             const unsigned tg = og / nx;
;             if (og + 1u == (tg + 1u) * nx) xb_add(&bar[XB_TOPGEN], 1u);
;             else XB_SPIN(xb_ld(&bar[XB_TOPGEN]) == tg, bar);
.LBB0_1147:
	s_or_b64 exec, exec, s[18:19]
	v_cvt_f32_u32_e32 v3, v0
	s_waitcnt vmcnt(0)
	buffer_inv sc1
	v_readfirstlane_b32 s2, v2
	s_add_u32 s18, s84, 0x7500
	s_addc_u32 s19, s85, 0
	v_rcp_iflag_f32_e32 v3, v3
	v_add_u32_e32 v1, s2, v1
	v_add_u32_e32 v4, 1, v1
	s_mov_b64 s[20:21], -1
	v_mul_f32_e32 v2, 0x4f7ffffe, v3
	v_cvt_u32_f32_e32 v2, v2
	v_sub_u32_e32 v3, 0, v0
	v_mul_lo_u32 v3, v3, v2
	v_mul_hi_u32 v3, v2, v3
	v_add_u32_e32 v2, v2, v3
	v_mul_hi_u32 v2, v1, v2
	v_mul_lo_u32 v3, v2, v0
	v_sub_u32_e32 v1, v1, v3
	v_add_u32_e32 v5, 1, v2
	v_cmp_ge_u32_e32 vcc, v1, v0
	v_sub_u32_e32 v3, v1, v0
	s_nop 0
	v_cndmask_b32_e32 v2, v2, v5, vcc
	v_cndmask_b32_e32 v1, v1, v3, vcc
	v_add_u32_e32 v3, 1, v2
	v_cmp_ge_u32_e32 vcc, v1, v0
	s_nop 1
	v_cndmask_b32_e32 v2, v2, v3, vcc
	v_mul_lo_u32 v1, v0, v2
	v_add_u32_e32 v0, v1, v0
	v_cmp_ne_u32_e32 vcc, v4, v0
	v_mov_b64_e32 v[0:1], s[18:19]
	s_and_saveexec_b64 s[16:17], vcc
	s_cbranch_execz .LBB0_1159
	v_mov_b32_e32 v0, 0
	global_load_dword v1, v0, s[18:19] sc1
	s_mov_b64 s[24:25], 0
	s_waitcnt vmcnt(0)
	v_cmp_eq_u32_e32 vcc, v1, v2
	s_and_saveexec_b64 s[22:23], vcc
	s_cbranch_execz .LBB0_1158
	s_add_u32 s20, s84, 0x4200
	s_addc_u32 s21, s85, 0
	s_mov_b32 s2, 1
	s_branch .LBB0_1151

; __device__ __forceinline__ unsigned xb_ld(unsigned* p)              { return __hip_atomic_load(p, __ATOMIC_RELAXED, __HIP_MEMORY_SCOPE_AGENT); }
; __device__ __forceinline__ unsigned xb_add(unsigned* p, unsigned v) { return __hip_atomic_fetch_add(p, v, __ATOMIC_RELAXED, __HIP_MEMORY_SCOPE_AGENT); }
; #define XB_SPIN(cond, bar) do { unsigned _sp = 0; while (cond) { __builtin_amdgcn_s_sleep(1); \
;     if ((++_sp & 255u) == 0u) { if (xb_ld(&(bar)[XB_TMO])) break; if (_sp > XB_SPIN_CAP) { atomicAdd(&(bar)[XB_TMO], 1u); break; } } } } while (0)
; __device__ __forceinline__ void xcd_barrier(const XcdBarrier& b, int tid) {
;     ...
;             else XB_SPIN(xb_ld(&bar[XB_TOPGEN]) == tg, bar);
;             __builtin_amdgcn_fence(__ATOMIC_ACQUIRE, "agent");
;             xb_add(&bar[XB_XGEN(b.x)], 1u);
;             asm volatile("s_waitcnt vmcnt(0)" ::: "memory");
.LBB0_1161:
	s_or_b64 exec, exec, s[16:17]
	v_mov_b32_e32 v0, 0x2000
	v_mov_b32_e32 v1, 1
	s_waitcnt vmcnt(0)
	global_atomic_add v0, v1, s[6:7] offset:1024
	s_waitcnt vmcnt(0)

; __device__ __forceinline__ unsigned xb_ld(unsigned* p)              { return __hip_atomic_load(p, __ATOMIC_RELAXED, __HIP_MEMORY_SCOPE_AGENT); }
; __device__ __forceinline__ unsigned xb_add(unsigned* p, unsigned v) { return __hip_atomic_fetch_add(p, v, __ATOMIC_RELAXED, __HIP_MEMORY_SCOPE_AGENT); }
; #define XB_SPIN(cond, bar) do { unsigned _sp = 0; while (cond) { __builtin_amdgcn_s_sleep(1); \
;     if ((++_sp & 255u) == 0u) { if (xb_ld(&(bar)[XB_TMO])) break; if (_sp > XB_SPIN_CAP) { atomicAdd(&(bar)[XB_TMO], 1u); break; } } } } while (0)
; __device__ __forceinline__ void xcd_barrier(const XcdBarrier& b, int tid) {
;     ...
;         const unsigned old = xb_add(&bar[XB_XSUB(b.x)], 1u);
;         const unsigned gen = old / nloc;
;         if (old + 1u == (gen + 1u) * nloc) {
;             __builtin_amdgcn_fence(__ATOMIC_RELEASE, "agent");
;             asm volatile("s_waitcnt vmcnt(0)" ::: "memory");
;             const unsigned og = xb_add(&bar[XB_TOP], 1u);
;             const unsigned tg = og / nx;
;             if (og + 1u == (tg + 1u) * nx) xb_add(&bar[XB_TOPGEN], 1u);
;             else XB_SPIN(xb_ld(&bar[XB_TOPGEN]) == tg, bar);
;             __builtin_amdgcn_fence(__ATOMIC_ACQUIRE, "agent");
;             xb_add(&bar[XB_XGEN(b.x)], 1u);
;             asm volatile("s_waitcnt vmcnt(0)" ::: "memory");
;         } else {
;             XB_SPIN(xb_ld(&bar[XB_XGEN(b.x)]) == gen, bar);
;             __builtin_amdgcn_fence(__ATOMIC_ACQUIRE, "agent");
;             asm volatile("s_waitcnt vmcnt(0)" ::: "memory");
;         }
.LBB0_1232:
	v_readlane_b32 s2, v249, 2
	s_lshl_b32 s2, s2, 8
	v_readlane_b32 s6, v249, 3
	v_readlane_b32 s7, v249, 4
	s_add_u32 s6, s6, s2
	s_addc_u32 s7, s7, 0
	v_mov_b32_e32 v1, 0x1000
	v_mov_b32_e32 v3, 1
	v_sub_u32_e32 v4, 0, v2
	global_atomic_add v3, v1, v3, s[6:7] offset:1024 sc0
	v_cvt_f32_u32_e32 v1, v2
	v_rcp_iflag_f32_e32 v1, v1
	s_nop 0
	v_mul_f32_e32 v1, 0x4f7ffffe, v1
	v_cvt_u32_f32_e32 v1, v1
	v_mul_lo_u32 v4, v4, v1
	v_mul_hi_u32 v4, v1, v4
	v_add_u32_e32 v1, v1, v4
	s_waitcnt vmcnt(0)
	v_mul_hi_u32 v1, v3, v1
	v_mul_lo_u32 v4, v1, v2
	v_sub_u32_e32 v4, v3, v4
	v_add_u32_e32 v5, 1, v1
	v_cmp_ge_u32_e32 vcc, v4, v2
	v_add_u32_e32 v3, 1, v3
	s_nop 0
	v_cndmask_b32_e32 v1, v1, v5, vcc
	v_sub_u32_e32 v5, v4, v2
	v_cndmask_b32_e32 v4, v4, v5, vcc
	v_add_u32_e32 v5, 1, v1
	v_cmp_ge_u32_e32 vcc, v4, v2
	s_nop 1
	v_cndmask_b32_e32 v1, v1, v5, vcc
	v_mul_lo_u32 v4, v2, v1
	v_add_u32_e32 v2, v4, v2
	v_cmp_ne_u32_e32 vcc, v3, v2
	s_and_saveexec_b64 s[2:3], vcc
	s_xor_b64 s[8:9], exec, s[2:3]
	s_cbranch_execz .LBB0_1246
	s_waitcnt lgkmcnt(0)
	buffer_inv sc1
	v_mov_b32_e32 v0, 0x2000
	global_load_dword v0, v0, s[6:7] offset:1024 sc1
	s_add_u32 s18, s6, 0x2400
	s_addc_u32 s19, s7, 0
	s_waitcnt vmcnt(0)
	v_cmp_eq_u32_e32 vcc, v0, v1
	s_and_saveexec_b64 s[10:11], vcc
	s_cbranch_execz .LBB0_1245
	s_add_u32 s16, s84, 0x4200
	s_addc_u32 s17, s85, 0
	s_mov_b32 s2, 1
	s_mov_b64 s[20:21], 0
	v_mov_b32_e32 v0, 0
	s_branch .LBB0_1236

; __device__ __forceinline__ unsigned xb_ld(unsigned* p)              { return __hip_atomic_load(p, __ATOMIC_RELAXED, __HIP_MEMORY_SCOPE_AGENT); }
; #define XB_SPIN(cond, bar) do { unsigned _sp = 0; while (cond) { __builtin_amdgcn_s_sleep(1); \
;     if ((++_sp & 255u) == 0u) { if (xb_ld(&(bar)[XB_TMO])) break; if (_sp > XB_SPIN_CAP) { atomicAdd(&(bar)[XB_TMO], 1u); break; } } } } while (0)
; __device__ __forceinline__ void xcd_barrier(const XcdBarrier& b, int tid) {
;     ...
;             XB_SPIN(xb_ld(&bar[XB_XGEN(b.x)]) == gen, bar);
;             __builtin_amdgcn_fence(__ATOMIC_ACQUIRE, "agent");
;             asm volatile("s_waitcnt vmcnt(0)" ::: "memory");
.LBB0_1245:
	s_or_b64 exec, exec, s[10:11]
	s_waitcnt vmcnt(0)
	s_waitcnt vmcnt(0)

; __device__ __forceinline__ unsigned xb_ld(unsigned* p)              { return __hip_atomic_load(p, __ATOMIC_RELAXED, __HIP_MEMORY_SCOPE_AGENT); }
; __device__ __forceinline__ unsigned xb_add(unsigned* p, unsigned v) { return __hip_atomic_fetch_add(p, v, __ATOMIC_RELAXED, __HIP_MEMORY_SCOPE_AGENT); }
; #define XB_SPIN(cond, bar) do { unsigned _sp = 0; while (cond) { __builtin_amdgcn_s_sleep(1); \
;     if ((++_sp & 255u) == 0u) { if (xb_ld(&(bar)[XB_TMO])) break; if (_sp > XB_SPIN_CAP) { atomicAdd(&(bar)[XB_TMO], 1u); break; } } } } while (0)
; __device__ __forceinline__ void xcd_barrier(const XcdBarrier& b, int tid) {
;     ...
;         if (old + 1u == (gen + 1u) * nloc) {
;             __builtin_amdgcn_fence(__ATOMIC_RELEASE, "agent");
;             asm volatile("s_waitcnt vmcnt(0)" ::: "memory");
;             const unsigned og = xb_add(&bar[XB_TOP], 1u);
;             const unsigned tg = og / nx;
;             if (og + 1u == (tg + 1u) * nx) xb_add(&bar[XB_TOPGEN], 1u);
;             else XB_SPIN(xb_ld(&bar[XB_TOPGEN]) == tg, bar);
.LBB0_1249:
	s_or_b64 exec, exec, s[10:11]
	v_cvt_f32_u32_e32 v3, v0
	s_waitcnt vmcnt(0)
	buffer_inv sc1
	v_readfirstlane_b32 s2, v2
	s_add_u32 s10, s84, 0x7500
	s_addc_u32 s11, s85, 0
	v_rcp_iflag_f32_e32 v3, v3
	v_add_u32_e32 v1, s2, v1
	v_add_u32_e32 v4, 1, v1
	s_mov_b64 s[16:17], -1
	v_mul_f32_e32 v2, 0x4f7ffffe, v3
	v_cvt_u32_f32_e32 v2, v2
	v_sub_u32_e32 v3, 0, v0
	v_mul_lo_u32 v3, v3, v2
	v_mul_hi_u32 v3, v2, v3
	v_add_u32_e32 v2, v2, v3
	v_mul_hi_u32 v2, v1, v2
	v_mul_lo_u32 v3, v2, v0
	v_sub_u32_e32 v1, v1, v3
	v_add_u32_e32 v5, 1, v2
	v_cmp_ge_u32_e32 vcc, v1, v0
	v_sub_u32_e32 v3, v1, v0
	s_nop 0
	v_cndmask_b32_e32 v2, v2, v5, vcc
	v_cndmask_b32_e32 v1, v1, v3, vcc
	v_add_u32_e32 v3, 1, v2
	v_cmp_ge_u32_e32 vcc, v1, v0
	s_nop 1
	v_cndmask_b32_e32 v2, v2, v3, vcc
	v_mul_lo_u32 v1, v0, v2
	v_add_u32_e32 v0, v1, v0
	v_cmp_ne_u32_e32 vcc, v4, v0
	v_mov_b64_e32 v[0:1], s[10:11]
	s_and_saveexec_b64 s[8:9], vcc
	s_cbranch_execz .LBB0_1261
	v_mov_b32_e32 v0, 0
	global_load_dword v1, v0, s[10:11] sc1
	s_mov_b64 s[20:21], 0
	s_waitcnt vmcnt(0)
	v_cmp_eq_u32_e32 vcc, v1, v2
	s_and_saveexec_b64 s[18:19], vcc
	s_cbranch_execz .LBB0_1260
	s_add_u32 s16, s84, 0x4200
	s_addc_u32 s17, s85, 0
	s_mov_b32 s2, 1
	s_branch .LBB0_1253

; __device__ __forceinline__ unsigned xb_ld(unsigned* p)              { return __hip_atomic_load(p, __ATOMIC_RELAXED, __HIP_MEMORY_SCOPE_AGENT); }
; __device__ __forceinline__ unsigned xb_add(unsigned* p, unsigned v) { return __hip_atomic_fetch_add(p, v, __ATOMIC_RELAXED, __HIP_MEMORY_SCOPE_AGENT); }
; #define XB_SPIN(cond, bar) do { unsigned _sp = 0; while (cond) { __builtin_amdgcn_s_sleep(1); \
;     if ((++_sp & 255u) == 0u) { if (xb_ld(&(bar)[XB_TMO])) break; if (_sp > XB_SPIN_CAP) { atomicAdd(&(bar)[XB_TMO], 1u); break; } } } } while (0)
; __device__ __forceinline__ void xcd_barrier(const XcdBarrier& b, int tid) {
;     ...
;             else XB_SPIN(xb_ld(&bar[XB_TOPGEN]) == tg, bar);
;             __builtin_amdgcn_fence(__ATOMIC_ACQUIRE, "agent");
;             xb_add(&bar[XB_XGEN(b.x)], 1u);
;             asm volatile("s_waitcnt vmcnt(0)" ::: "memory");
.LBB0_1263:
	s_or_b64 exec, exec, s[8:9]
	v_mov_b32_e32 v0, 0x2000
	v_mov_b32_e32 v1, 1
	s_waitcnt vmcnt(0)
	global_atomic_add v0, v1, s[6:7] offset:1024
	s_waitcnt vmcnt(0)

; __device__ __forceinline__ unsigned xb_ld(unsigned* p)              { return __hip_atomic_load(p, __ATOMIC_RELAXED, __HIP_MEMORY_SCOPE_AGENT); }
; __device__ __forceinline__ unsigned xb_add(unsigned* p, unsigned v) { return __hip_atomic_fetch_add(p, v, __ATOMIC_RELAXED, __HIP_MEMORY_SCOPE_AGENT); }
; #define XB_SPIN(cond, bar) do { unsigned _sp = 0; while (cond) { __builtin_amdgcn_s_sleep(1); \
;     if ((++_sp & 255u) == 0u) { if (xb_ld(&(bar)[XB_TMO])) break; if (_sp > XB_SPIN_CAP) { atomicAdd(&(bar)[XB_TMO], 1u); break; } } } } while (0)
; __device__ __forceinline__ void xcd_barrier(const XcdBarrier& b, int tid) {
;     ...
;         const unsigned old = xb_add(&bar[XB_XSUB(b.x)], 1u);
;         const unsigned gen = old / nloc;
;         if (old + 1u == (gen + 1u) * nloc) {
;             __builtin_amdgcn_fence(__ATOMIC_RELEASE, "agent");
;             asm volatile("s_waitcnt vmcnt(0)" ::: "memory");
;             const unsigned og = xb_add(&bar[XB_TOP], 1u);
;             const unsigned tg = og / nx;
;             if (og + 1u == (tg + 1u) * nx) xb_add(&bar[XB_TOPGEN], 1u);
;             else XB_SPIN(xb_ld(&bar[XB_TOPGEN]) == tg, bar);
;             __builtin_amdgcn_fence(__ATOMIC_ACQUIRE, "agent");
;             xb_add(&bar[XB_XGEN(b.x)], 1u);
;             asm volatile("s_waitcnt vmcnt(0)" ::: "memory");
;         } else {
;             XB_SPIN(xb_ld(&bar[XB_XGEN(b.x)]) == gen, bar);
;             __builtin_amdgcn_fence(__ATOMIC_ACQUIRE, "agent");
;             asm volatile("s_waitcnt vmcnt(0)" ::: "memory");
;         }
.LBB0_1298:
	v_readlane_b32 s2, v249, 2
	s_lshl_b32 s2, s2, 8
	v_readlane_b32 s4, v249, 3
	v_readlane_b32 s5, v249, 4
	s_add_u32 s2, s4, s2
	s_addc_u32 s3, s5, 0
	v_mov_b32_e32 v1, 0x1000
	v_mov_b32_e32 v3, 1
	global_atomic_add v3, v1, v3, s[2:3] offset:1024 sc0
	v_cvt_f32_u32_e32 v1, v2
	v_sub_u32_e32 v4, 0, v2
	v_rcp_iflag_f32_e32 v1, v1
	s_nop 0
	v_mul_f32_e32 v1, 0x4f7ffffe, v1
	v_cvt_u32_f32_e32 v1, v1
	v_mul_lo_u32 v4, v4, v1
	v_mul_hi_u32 v4, v1, v4
	v_add_u32_e32 v1, v1, v4
	s_waitcnt vmcnt(0)
	v_mul_hi_u32 v1, v3, v1
	v_mul_lo_u32 v4, v1, v2
	v_sub_u32_e32 v4, v3, v4
	v_add_u32_e32 v5, 1, v1
	v_cmp_ge_u32_e32 vcc, v4, v2
	v_add_u32_e32 v3, 1, v3
	s_nop 0
	v_cndmask_b32_e32 v1, v1, v5, vcc
	v_sub_u32_e32 v5, v4, v2
	v_cndmask_b32_e32 v4, v4, v5, vcc
	v_add_u32_e32 v5, 1, v1
	v_cmp_ge_u32_e32 vcc, v4, v2
	s_nop 1
	v_cndmask_b32_e32 v1, v1, v5, vcc
	v_mul_lo_u32 v4, v2, v1
	v_add_u32_e32 v2, v4, v2
	v_cmp_ne_u32_e32 vcc, v3, v2
	s_and_saveexec_b64 s[4:5], vcc
	s_xor_b64 s[4:5], exec, s[4:5]
	s_cbranch_execz .LBB0_1312
	s_waitcnt lgkmcnt(0)
	buffer_inv sc1
	v_mov_b32_e32 v0, 0x2000
	global_load_dword v0, v0, s[2:3] offset:1024 sc1
	s_add_u32 s10, s2, 0x2400
	s_addc_u32 s11, s3, 0
	s_waitcnt vmcnt(0)
	v_cmp_eq_u32_e32 vcc, v0, v1
	s_and_saveexec_b64 s[6:7], vcc
	s_cbranch_execz .LBB0_1311
	s_add_u32 s8, s84, 0x4200
	s_addc_u32 s9, s85, 0
	s_mov_b32 s22, 1
	s_mov_b64 s[12:13], 0
	v_mov_b32_e32 v0, 0
	s_branch .LBB0_1302

; __device__ __forceinline__ unsigned xb_ld(unsigned* p)              { return __hip_atomic_load(p, __ATOMIC_RELAXED, __HIP_MEMORY_SCOPE_AGENT); }
; #define XB_SPIN(cond, bar) do { unsigned _sp = 0; while (cond) { __builtin_amdgcn_s_sleep(1); \
;     if ((++_sp & 255u) == 0u) { if (xb_ld(&(bar)[XB_TMO])) break; if (_sp > XB_SPIN_CAP) { atomicAdd(&(bar)[XB_TMO], 1u); break; } } } } while (0)
; __device__ __forceinline__ void xcd_barrier(const XcdBarrier& b, int tid) {
;     ...
;             XB_SPIN(xb_ld(&bar[XB_XGEN(b.x)]) == gen, bar);
;             __builtin_amdgcn_fence(__ATOMIC_ACQUIRE, "agent");
;             asm volatile("s_waitcnt vmcnt(0)" ::: "memory");
.LBB0_1311:
	s_or_b64 exec, exec, s[6:7]
	s_waitcnt vmcnt(0)
	s_waitcnt vmcnt(0)

; __device__ __forceinline__ unsigned xb_ld(unsigned* p)              { return __hip_atomic_load(p, __ATOMIC_RELAXED, __HIP_MEMORY_SCOPE_AGENT); }
; __device__ __forceinline__ unsigned xb_add(unsigned* p, unsigned v) { return __hip_atomic_fetch_add(p, v, __ATOMIC_RELAXED, __HIP_MEMORY_SCOPE_AGENT); }
; #define XB_SPIN(cond, bar) do { unsigned _sp = 0; while (cond) { __builtin_amdgcn_s_sleep(1); \
;     if ((++_sp & 255u) == 0u) { if (xb_ld(&(bar)[XB_TMO])) break; if (_sp > XB_SPIN_CAP) { atomicAdd(&(bar)[XB_TMO], 1u); break; } } } } while (0)
; __device__ __forceinline__ void xcd_barrier(const XcdBarrier& b, int tid) {
;     ...
;         if (old + 1u == (gen + 1u) * nloc) {
;             __builtin_amdgcn_fence(__ATOMIC_RELEASE, "agent");
;             asm volatile("s_waitcnt vmcnt(0)" ::: "memory");
;             const unsigned og = xb_add(&bar[XB_TOP], 1u);
;             const unsigned tg = og / nx;
;             if (og + 1u == (tg + 1u) * nx) xb_add(&bar[XB_TOPGEN], 1u);
;             else XB_SPIN(xb_ld(&bar[XB_TOPGEN]) == tg, bar);
.LBB0_1315:
	s_or_b64 exec, exec, s[6:7]
	v_cvt_f32_u32_e32 v3, v0
	s_waitcnt vmcnt(0)
	buffer_inv sc1
	v_readfirstlane_b32 s4, v2
	s_add_u32 s6, s84, 0x7500
	s_addc_u32 s7, s85, 0
	v_rcp_iflag_f32_e32 v3, v3
	v_add_u32_e32 v1, s4, v1
	v_add_u32_e32 v4, 1, v1
	s_mov_b64 s[8:9], -1
	v_mul_f32_e32 v2, 0x4f7ffffe, v3
	v_cvt_u32_f32_e32 v2, v2
	v_sub_u32_e32 v3, 0, v0
	v_mul_lo_u32 v3, v3, v2
	v_mul_hi_u32 v3, v2, v3
	v_add_u32_e32 v2, v2, v3
	v_mul_hi_u32 v2, v1, v2
	v_mul_lo_u32 v3, v2, v0
	v_sub_u32_e32 v1, v1, v3
	v_add_u32_e32 v5, 1, v2
	v_cmp_ge_u32_e32 vcc, v1, v0
	v_sub_u32_e32 v3, v1, v0
	s_nop 0
	v_cndmask_b32_e32 v2, v2, v5, vcc
	v_cndmask_b32_e32 v1, v1, v3, vcc
	v_add_u32_e32 v3, 1, v2
	v_cmp_ge_u32_e32 vcc, v1, v0
	s_nop 1
	v_cndmask_b32_e32 v2, v2, v3, vcc
	v_mul_lo_u32 v1, v0, v2
	v_add_u32_e32 v0, v1, v0
	v_cmp_ne_u32_e32 vcc, v4, v0
	v_mov_b64_e32 v[0:1], s[6:7]
	s_and_saveexec_b64 s[4:5], vcc
	s_cbranch_execz .LBB0_1327
	v_mov_b32_e32 v0, 0
	global_load_dword v1, v0, s[6:7] sc1
	s_mov_b64 s[12:13], 0
	s_waitcnt vmcnt(0)
	v_cmp_eq_u32_e32 vcc, v1, v2
	s_and_saveexec_b64 s[10:11], vcc
	s_cbranch_execz .LBB0_1326
	s_add_u32 s8, s84, 0x4200
	s_addc_u32 s9, s85, 0
	s_mov_b32 s22, 1
	s_branch .LBB0_1319

; __device__ __forceinline__ unsigned xb_ld(unsigned* p)              { return __hip_atomic_load(p, __ATOMIC_RELAXED, __HIP_MEMORY_SCOPE_AGENT); }
; __device__ __forceinline__ unsigned xb_add(unsigned* p, unsigned v) { return __hip_atomic_fetch_add(p, v, __ATOMIC_RELAXED, __HIP_MEMORY_SCOPE_AGENT); }
; #define XB_SPIN(cond, bar) do { unsigned _sp = 0; while (cond) { __builtin_amdgcn_s_sleep(1); \
;     if ((++_sp & 255u) == 0u) { if (xb_ld(&(bar)[XB_TMO])) break; if (_sp > XB_SPIN_CAP) { atomicAdd(&(bar)[XB_TMO], 1u); break; } } } } while (0)
; __device__ __forceinline__ void xcd_barrier(const XcdBarrier& b, int tid) {
;     ...
;             else XB_SPIN(xb_ld(&bar[XB_TOPGEN]) == tg, bar);
;             __builtin_amdgcn_fence(__ATOMIC_ACQUIRE, "agent");
;             xb_add(&bar[XB_XGEN(b.x)], 1u);
;             asm volatile("s_waitcnt vmcnt(0)" ::: "memory");
.LBB0_1329:
	s_or_b64 exec, exec, s[4:5]
	v_mov_b32_e32 v0, 0x2000
	v_mov_b32_e32 v1, 1
	s_waitcnt vmcnt(0)
	global_atomic_add v0, v1, s[2:3] offset:1024
	s_waitcnt vmcnt(0)
